# speedup vs baseline: 1.0181x; 1.0028x over previous
.LBB0_26:
	v_and_b32_e32 v2, 63, v0
	v_lshrrev_b32_e32 v3, 6, v0
	v_lshrrev_b32_e32 v4, 3, v2
	v_lshlrev_b32_e32 v4, 6, v4
	v_lshl_or_b32 v4, v3, 4, v4
	v_and_b32_e32 v6, 7, v2
	v_lshl_or_b32 v4, v6, 1, v4
	s_mov_b32 s0, 0x41800000
	v_fma_mixlo_f16 v16, v51, s0, 0
	v_fma_mixlo_f16 v20, v50, s0, 0
	v_fma_mixlo_f16 v17, v49, s0, 0
	v_fma_mixlo_f16 v21, v48, s0, 0
	v_fma_mixlo_f16 v18, v47, s0, 0
	v_fma_mixlo_f16 v22, v46, s0, 0
	v_fma_mixlo_f16 v19, v45, s0, 0
	v_fma_mixlo_f16 v23, v5, s0, 0
	s_waitcnt lgkmcnt(0)
	s_barrier
	ds_write_b16 v4, v16
	ds_write_b16 v4, v20 offset:2048
	ds_write_b16 v4, v17 offset:512
	ds_write_b16 v4, v21 offset:2560
	ds_write_b16 v4, v18 offset:1024
	ds_write_b16 v4, v22 offset:3072
	ds_write_b16 v4, v19 offset:1536
	ds_write_b16 v4, v23 offset:3584
	v_lshlrev_b32_e32 v7, 4, v2
	v_lshl_or_b32 v7, v3, 10, v7
	v_lshrrev_b32_e32 v12, 2, v2
	v_lshl_or_b32 v12, v3, 4, v12
	v_lshlrev_b32_e32 v12, 15, v12
	v_sub_u32_e32 v13, v1, v3
	v_and_b32_e32 v14, 3, v2
	v_add_u32_e32 v13, v13, v14
	v_lshl_add_u32 v12, v13, 4, v12
	s_waitcnt lgkmcnt(0)
	s_barrier
	ds_read_b128 v[8:11], v7
	s_waitcnt lgkmcnt(0)
	global_store_dwordx4 v12, v[8:11], s[12:13] sc0 sc1
	s_endpgm
